# speedup vs baseline: 1.0069x; 1.0069x over previous
.LBB1_12:
	s_mov_b64 s[36:37], 0x80
	s_add_i32 m0, s57, 0x18000
	v_lshl_add_u64 v[12:13], v[12:13], 0, s[36:37]
	global_load_lds_dwordx4 v[12:13], off
	v_lshl_add_u64 v[10:11], v[10:11], 0, s[36:37]
	s_add_i32 m0, s57, 0x1a000
	s_add_i32 s62, s57, 0x8000
	global_load_lds_dwordx4 v[10:11], off
	v_lshl_add_u64 v[8:9], v[8:9], 0, s[36:37]
	s_mov_b32 m0, s62
	s_add_i32 s63, s57, 0xa000
	global_load_lds_dwordx4 v[8:9], off
	v_lshl_add_u64 v[6:7], v[6:7], 0, s[36:37]
	s_mov_b32 m0, s63
	v_lshl_add_u64 v[4:5], v[4:5], 0, s[36:37]
	global_load_lds_dwordx4 v[6:7], off
	s_add_i32 m0, s57, 0x1c000
	v_lshl_add_u64 v[2:3], v[2:3], 0, s[36:37]
	global_load_lds_dwordx4 v[4:5], off
	s_add_i32 m0, s57, 0x1e000
	s_lshr_b32 s7, s7, 26
	global_load_lds_dwordx4 v[2:3], off
	s_waitcnt vmcnt(8)
	s_barrier
	s_and_b32 s5, s0, 3
	s_add_i32 s7, s6, s7
	s_ashr_i32 s61, s7, 6
	s_lshl_b32 s55, s1, 6
	s_lshl_b32 s1, s1, 13
	s_lshl_b32 s54, s5, 5
	s_cmp_gt_i32 s6, 63
	s_cselect_b64 s[38:39], -1, 0
	s_lshl_b32 s66, s40, 3
	s_lshl_b32 s0, s0, 3
	v_lshlrev_b32_e32 v2, 1, v1
	s_abs_i32 s67, s66
	v_and_or_b32 v144, s0, 8, v2
	v_cvt_f32_u32_e32 v2, s67
	v_lshlrev_b32_e32 v20, 2, v168
	v_lshl_or_b32 v19, v168, 6, v169
	v_and_b32_e32 v20, 32, v20
	v_rcp_iflag_f32_e32 v2, v2
	v_bitop3_b32 v19, v19, s1, v20 bitop3:0xde
	v_lshl_or_b32 v143, s5, 12, v173
	s_ashr_i32 s5, s4, 31
	v_mul_f32_e32 v2, 0x4f7ffffe, v2
	v_cvt_u32_f32_e32 v2, v2
	v_lshlrev_b32_e32 v66, 4, v144
	v_lshl_add_u64 v[154:155], s[22:23], 0, v[66:67]
	s_lshr_b32 s0, s5, 29
	v_readfirstlane_b32 s1, v2
	v_add_u32_e32 v2, v18, v16
	v_mul_lo_u32 v2, s6, v2
	v_lshlrev_b32_e32 v2, 1, v2
	v_add3_u32 v66, v14, v2, v15
	v_add_u32_e32 v2, v17, v16
	s_add_i32 s0, s4, s0
	v_mul_lo_u32 v2, s6, v2
	s_ashr_i32 s68, s0, 3
	s_and_b32 s0, s0, -8
	v_lshlrev_b32_e32 v2, 1, v2
	s_sub_i32 s69, s4, s0
	s_sub_i32 s0, 0, s67
	v_lshl_add_u64 v[156:157], s[30:31], 0, v[66:67]
	v_add3_u32 v66, v14, v2, v15
	s_waitcnt vmcnt(6)
	s_mul_i32 s0, s0, s1
	v_lshl_add_u64 v[158:159], s[30:31], 0, v[66:67]
	v_mov_b32_e32 v66, v67
	v_mov_b32_e32 v68, v67
	v_mov_b32_e32 v69, v67
	s_add_i32 s70, s68, 1
	s_mul_hi_u32 s0, s1, s0
	v_add_u32_e32 v145, 0, v19
	v_mov_b64_e32 v[2:3], v[66:67]
	v_mov_b64_e32 v[6:7], v[66:67]
	v_mov_b64_e32 v[18:19], v[66:67]
	v_mov_b64_e32 v[22:23], v[66:67]
	v_mov_b64_e32 v[34:35], v[66:67]
	v_mov_b64_e32 v[38:39], v[66:67]
	v_mov_b64_e32 v[50:51], v[66:67]
	v_mov_b64_e32 v[54:55], v[66:67]
	v_mov_b64_e32 v[10:11], v[66:67]
	v_mov_b64_e32 v[14:15], v[66:67]
	v_mov_b64_e32 v[26:27], v[66:67]
	v_mov_b64_e32 v[30:31], v[66:67]
	v_mov_b64_e32 v[42:43], v[66:67]
	v_mov_b64_e32 v[46:47], v[66:67]
	v_mov_b64_e32 v[58:59], v[66:67]
	v_mov_b64_e32 v[62:63], v[66:67]
	v_mov_b64_e32 v[72:73], v[68:69]
	v_mov_b64_e32 v[76:77], v[68:69]
	v_mov_b64_e32 v[88:89], v[68:69]
	v_mov_b64_e32 v[92:93], v[68:69]
	v_mov_b64_e32 v[104:105], v[68:69]
	v_mov_b64_e32 v[108:109], v[68:69]
	v_mov_b64_e32 v[120:121], v[68:69]
	v_mov_b64_e32 v[124:125], v[68:69]
	v_mov_b64_e32 v[80:81], v[68:69]
	v_mov_b64_e32 v[84:85], v[68:69]
	v_mov_b64_e32 v[96:97], v[68:69]
	v_mov_b64_e32 v[100:101], v[68:69]
	v_mov_b64_e32 v[112:113], v[68:69]
	v_mov_b64_e32 v[116:117], v[68:69]
	v_mov_b64_e32 v[128:129], v[68:69]
	v_mov_b64_e32 v[132:133], v[68:69]
	s_add_i32 s65, s61, -2
	v_lshlrev_b32_e32 v142, 3, v168
	s_ashr_i32 s64, s2, 31
	s_mul_i32 s71, s70, s69
	s_bfe_i32 s72, s40, 0x1001c
	s_add_i32 s73, s1, s0
	v_mov_b64_e32 v[160:161], s[4:5]
	s_add_i32 s74, 0, 0x10000
	s_add_i32 s75, 0, 0x14000
	v_mov_b64_e32 v[4:5], v[68:69]
	v_mov_b64_e32 v[8:9], v[68:69]
	v_mov_b64_e32 v[20:21], v[68:69]
	v_mov_b64_e32 v[24:25], v[68:69]
	v_mov_b64_e32 v[36:37], v[68:69]
	v_mov_b64_e32 v[40:41], v[68:69]
	v_mov_b64_e32 v[52:53], v[68:69]
	v_mov_b64_e32 v[56:57], v[68:69]
	v_mov_b64_e32 v[12:13], v[68:69]
	v_mov_b64_e32 v[16:17], v[68:69]
	v_mov_b64_e32 v[28:29], v[68:69]
	v_mov_b64_e32 v[32:33], v[68:69]
	v_mov_b64_e32 v[44:45], v[68:69]
	v_mov_b64_e32 v[48:49], v[68:69]
	v_mov_b64_e32 v[60:61], v[68:69]
	v_mov_b64_e32 v[64:65], v[68:69]
	v_mov_b64_e32 v[70:71], v[66:67]
	v_mov_b64_e32 v[74:75], v[66:67]
	v_mov_b64_e32 v[86:87], v[66:67]
	v_mov_b64_e32 v[90:91], v[66:67]
	v_mov_b64_e32 v[102:103], v[66:67]
	v_mov_b64_e32 v[106:107], v[66:67]
	v_mov_b64_e32 v[118:119], v[66:67]
	v_mov_b64_e32 v[122:123], v[66:67]
	v_mov_b64_e32 v[78:79], v[66:67]
	v_mov_b64_e32 v[82:83], v[66:67]
	v_mov_b64_e32 v[94:95], v[66:67]
	v_mov_b64_e32 v[98:99], v[66:67]
	v_mov_b64_e32 v[110:111], v[66:67]
	v_mov_b64_e32 v[114:115], v[66:67]
	v_mov_b64_e32 v[126:127], v[66:67]
	v_mov_b64_e32 v[130:131], v[66:67]
	s_barrier
